# NSA compression MFMA chain: 16 B-fragment global loads and 8 A-fragment LDS reads in flight (counted waits) instead of ~5; on top of rt9
# speedup vs baseline: 1.0076x; 1.0027x over previous
; #define CMP_LOADW(dst, lb) { _Pragma("unroll") for (int q = 0; q < 4; ++q) _Pragma("unroll") for (int ks = 0; ks < 4; ++ks) dst[q][ks] = *(const GAS bf16x8*)(wrow + ((lb) + q) * 64 + 16 * ks); }
; #define CMP_MMA(src, lb) { _Pragma("unroll") for (int q = 0; q < 4; ++q) { const int ll = (lb) + q; const LAS unsigned char* xr = XS + ((ll & 15) * 33 + (ll >> 4) + r32) * XP + 16 * h; \
;             _Pragma("unroll") for (int ks = 0; ks < 4; ++ks) { const bf16x8 af = *(const LAS bf16x8*)(xr + 32 * ks); acc = __builtin_amdgcn_mfma_f32_32x32x16_bf16(af, src[q][ks], acc, 0, 0, 0); } } }
; __device__ __forceinline__ void compress_mfma_phase(Frame& F, int l, bf16* CMP) {
;     ...
;         const int ct = w & 3, lh = w >> 2;
;         f32x16 acc;
; #pragma unroll
;         for (int i = 0; i < 16; ++i) acc[i] = 0.f;
;         const bf16* wrow = W1T + (size_t)(32 * ct + r32) * 2048 + 8 * h;
;         { bf16x8 wa[4][4], wb[4][4]; const int l0 = 16 * lh;
;     ...
;           CMP_LOADW(wa, l0) CMP_LOADW(wb, l0 + 4) CMP_MMA(wa, l0) CMP_LOADW(wa, l0 + 8) CMP_MMA(wb, l0 + 4) CMP_LOADW(wb, l0 + 12) CMP_MMA(wa, l0 + 8) CMP_MMA(wb, l0 + 12)
.LBB0_379:
	s_or_b64 exec, exec, s[0:1]
	s_ashr_i32 s0, s73, 7
	s_ashr_i32 s1, s0, 31
	s_lshl_b64 s[2:3], s[0:1], 19
	s_waitcnt vmcnt(0)
	v_lshl_add_u64 v[18:19], v[38:39], 0, s[2:3]
	s_waitcnt lgkmcnt(0)
	s_barrier
	global_load_dwordx4 v[138:141], v[18:19], off
	global_load_dwordx4 v[142:145], v[18:19], off offset:32
	global_load_dwordx4 v[146:149], v[18:19], off offset:64
	global_load_dwordx4 v[150:153], v[18:19], off offset:96
	global_load_dwordx4 v[154:157], v[18:19], off offset:128
	global_load_dwordx4 v[158:161], v[18:19], off offset:160
	global_load_dwordx4 v[162:165], v[18:19], off offset:192
	global_load_dwordx4 v[166:169], v[18:19], off offset:224
	global_load_dwordx4 v[170:173], v[18:19], off offset:256
	global_load_dwordx4 v[174:177], v[18:19], off offset:288
	global_load_dwordx4 v[178:181], v[18:19], off offset:320
	global_load_dwordx4 v[182:185], v[18:19], off offset:352
	global_load_dwordx4 v[186:189], v[18:19], off offset:384
	global_load_dwordx4 v[190:193], v[18:19], off offset:416
	global_load_dwordx4 v[200:203], v[18:19], off offset:448
	global_load_dwordx4 v[204:207], v[18:19], off offset:480
	ds_read_b128 v[208:211], v48
	ds_read_b128 v[212:215], v48 offset:32
	ds_read_b128 v[216:219], v48 offset:64
	ds_read_b128 v[80:83], v48 offset:96
	ds_read_b128 v[84:87], v48 offset:4752
	ds_read_b128 v[88:91], v48 offset:4784
	ds_read_b128 v[92:95], v48 offset:4816
	ds_read_b128 v[96:99], v48 offset:4848
	s_waitcnt vmcnt(15) lgkmcnt(7)
	v_mfma_f32_32x32x16_bf16 v[2:17], v[208:211], v[138:141], 0
	global_load_dwordx4 v[138:141], v[18:19], off offset:512
	ds_read_b128 v[208:211], v48 offset:9504
	s_waitcnt vmcnt(15) lgkmcnt(7)
	v_mfma_f32_32x32x16_bf16 v[2:17], v[212:215], v[142:145], v[2:17]
	global_load_dwordx4 v[142:145], v[18:19], off offset:544
	ds_read_b128 v[212:215], v48 offset:9536
	s_waitcnt vmcnt(15) lgkmcnt(7)
	v_mfma_f32_32x32x16_bf16 v[2:17], v[216:219], v[146:149], v[2:17]
	global_load_dwordx4 v[146:149], v[18:19], off offset:576
	ds_read_b128 v[216:219], v48 offset:9568
	s_waitcnt vmcnt(15) lgkmcnt(7)
	v_mfma_f32_32x32x16_bf16 v[2:17], v[80:83], v[150:153], v[2:17]
	global_load_dwordx4 v[150:153], v[18:19], off offset:608
	ds_read_b128 v[80:83], v48 offset:9600
	s_waitcnt vmcnt(15) lgkmcnt(7)
	v_mfma_f32_32x32x16_bf16 v[2:17], v[84:87], v[154:157], v[2:17]
	global_load_dwordx4 v[154:157], v[18:19], off offset:640
	ds_read_b128 v[84:87], v48 offset:14256
	s_waitcnt vmcnt(15) lgkmcnt(7)
	v_mfma_f32_32x32x16_bf16 v[2:17], v[88:91], v[158:161], v[2:17]
	global_load_dwordx4 v[158:161], v[18:19], off offset:672
	ds_read_b128 v[88:91], v48 offset:14288
	s_waitcnt vmcnt(15) lgkmcnt(7)
	v_mfma_f32_32x32x16_bf16 v[2:17], v[92:95], v[162:165], v[2:17]
	global_load_dwordx4 v[162:165], v[18:19], off offset:704
	ds_read_b128 v[92:95], v48 offset:14320
	s_waitcnt vmcnt(15) lgkmcnt(7)
	v_mfma_f32_32x32x16_bf16 v[2:17], v[96:99], v[166:169], v[2:17]
	global_load_dwordx4 v[166:169], v[18:19], off offset:736
	ds_read_b128 v[96:99], v48 offset:14352
	s_waitcnt vmcnt(15) lgkmcnt(7)
	v_mfma_f32_32x32x16_bf16 v[2:17], v[208:211], v[170:173], v[2:17]
	global_load_dwordx4 v[170:173], v[18:19], off offset:768
	ds_read_b128 v[208:211], v48 offset:19008
	s_waitcnt vmcnt(15) lgkmcnt(7)
	v_mfma_f32_32x32x16_bf16 v[2:17], v[212:215], v[174:177], v[2:17]
	global_load_dwordx4 v[174:177], v[18:19], off offset:800
	ds_read_b128 v[212:215], v48 offset:19040
	s_waitcnt vmcnt(15) lgkmcnt(7)
	v_mfma_f32_32x32x16_bf16 v[2:17], v[216:219], v[178:181], v[2:17]
	global_load_dwordx4 v[178:181], v[18:19], off offset:832
	ds_read_b128 v[216:219], v48 offset:19072
	s_waitcnt vmcnt(15) lgkmcnt(7)
	v_mfma_f32_32x32x16_bf16 v[2:17], v[80:83], v[182:185], v[2:17]
	global_load_dwordx4 v[182:185], v[18:19], off offset:864
	ds_read_b128 v[80:83], v48 offset:19104
	s_waitcnt vmcnt(15) lgkmcnt(7)
	v_mfma_f32_32x32x16_bf16 v[2:17], v[84:87], v[186:189], v[2:17]
	global_load_dwordx4 v[186:189], v[18:19], off offset:896
	ds_read_b128 v[84:87], v48 offset:23760
	s_waitcnt vmcnt(15) lgkmcnt(7)
	v_mfma_f32_32x32x16_bf16 v[2:17], v[88:91], v[190:193], v[2:17]
	global_load_dwordx4 v[190:193], v[18:19], off offset:928
	ds_read_b128 v[88:91], v48 offset:23792
	s_waitcnt vmcnt(15) lgkmcnt(7)
	v_mfma_f32_32x32x16_bf16 v[2:17], v[92:95], v[200:203], v[2:17]
	global_load_dwordx4 v[200:203], v[18:19], off offset:960
	ds_read_b128 v[92:95], v48 offset:23824
	s_waitcnt vmcnt(15) lgkmcnt(7)
	v_mfma_f32_32x32x16_bf16 v[2:17], v[96:99], v[204:207], v[2:17]
	global_load_dwordx4 v[204:207], v[18:19], off offset:992
	ds_read_b128 v[96:99], v48 offset:23856
	s_waitcnt vmcnt(15) lgkmcnt(7)
	v_mfma_f32_32x32x16_bf16 v[2:17], v[208:211], v[138:141], v[2:17]
	global_load_dwordx4 v[138:141], v[18:19], off offset:1024
	ds_read_b128 v[208:211], v48 offset:28512
	s_waitcnt vmcnt(15) lgkmcnt(7)
	v_mfma_f32_32x32x16_bf16 v[2:17], v[212:215], v[142:145], v[2:17]
	global_load_dwordx4 v[142:145], v[18:19], off offset:1056
	ds_read_b128 v[212:215], v48 offset:28544
	s_waitcnt vmcnt(15) lgkmcnt(7)
	v_mfma_f32_32x32x16_bf16 v[2:17], v[216:219], v[146:149], v[2:17]
	global_load_dwordx4 v[146:149], v[18:19], off offset:1088
	ds_read_b128 v[216:219], v48 offset:28576
	s_waitcnt vmcnt(15) lgkmcnt(7)
	v_mfma_f32_32x32x16_bf16 v[2:17], v[80:83], v[150:153], v[2:17]
	global_load_dwordx4 v[150:153], v[18:19], off offset:1120
	ds_read_b128 v[80:83], v48 offset:28608
	s_waitcnt vmcnt(15) lgkmcnt(7)
	v_mfma_f32_32x32x16_bf16 v[2:17], v[84:87], v[154:157], v[2:17]
	global_load_dwordx4 v[154:157], v[18:19], off offset:1152
	ds_read_b128 v[84:87], v48 offset:33264
	s_waitcnt vmcnt(15) lgkmcnt(7)
; #define CMP_LOADW(dst, lb) { _Pragma("unroll") for (int q = 0; q < 4; ++q) _Pragma("unroll") for (int ks = 0; ks < 4; ++ks) dst[q][ks] = *(const GAS bf16x8*)(wrow + ((lb) + q) * 64 + 16 * ks); }
; #define CMP_MMA(src, lb) { _Pragma("unroll") for (int q = 0; q < 4; ++q) { const int ll = (lb) + q; const LAS unsigned char* xr = XS + ((ll & 15) * 33 + (ll >> 4) + r32) * XP + 16 * h; \
;             _Pragma("unroll") for (int ks = 0; ks < 4; ++ks) { const bf16x8 af = *(const LAS bf16x8*)(xr + 32 * ks); acc = __builtin_amdgcn_mfma_f32_32x32x16_bf16(af, src[q][ks], acc, 0, 0, 0); } } }
; __device__ __forceinline__ void compress_mfma_phase(Frame& F, int l, bf16* CMP) {
;     ...
;         { bf16x8 wa[4][4], wb[4][4]; const int l0 = 16 * lh;
;     ...
;           CMP_LOADW(wa, l0) CMP_LOADW(wb, l0 + 4) CMP_MMA(wa, l0) CMP_LOADW(wa, l0 + 8) CMP_MMA(wb, l0 + 4) CMP_LOADW(wb, l0 + 12) CMP_MMA(wa, l0 + 8) CMP_MMA(wb, l0 + 12)
	v_mfma_f32_32x32x16_bf16 v[2:17], v[88:91], v[158:161], v[2:17]
	global_load_dwordx4 v[158:161], v[18:19], off offset:1184
	ds_read_b128 v[88:91], v48 offset:33296
	s_waitcnt vmcnt(15) lgkmcnt(7)
	v_mfma_f32_32x32x16_bf16 v[2:17], v[92:95], v[162:165], v[2:17]
	global_load_dwordx4 v[162:165], v[18:19], off offset:1216
	ds_read_b128 v[92:95], v48 offset:33328
	s_waitcnt vmcnt(15) lgkmcnt(7)
	v_mfma_f32_32x32x16_bf16 v[2:17], v[96:99], v[166:169], v[2:17]
	global_load_dwordx4 v[166:169], v[18:19], off offset:1248
	ds_read_b128 v[96:99], v48 offset:33360
	s_waitcnt vmcnt(15) lgkmcnt(7)
	v_mfma_f32_32x32x16_bf16 v[2:17], v[208:211], v[170:173], v[2:17]
	global_load_dwordx4 v[170:173], v[18:19], off offset:1280
	ds_read_b128 v[208:211], v48 offset:38016
	s_waitcnt vmcnt(15) lgkmcnt(7)
	v_mfma_f32_32x32x16_bf16 v[2:17], v[212:215], v[174:177], v[2:17]
	global_load_dwordx4 v[174:177], v[18:19], off offset:1312
	ds_read_b128 v[212:215], v48 offset:38048
	s_waitcnt vmcnt(15) lgkmcnt(7)
	v_mfma_f32_32x32x16_bf16 v[2:17], v[216:219], v[178:181], v[2:17]
	global_load_dwordx4 v[178:181], v[18:19], off offset:1344
	ds_read_b128 v[216:219], v48 offset:38080
	s_waitcnt vmcnt(15) lgkmcnt(7)
	v_mfma_f32_32x32x16_bf16 v[2:17], v[80:83], v[182:185], v[2:17]
	global_load_dwordx4 v[182:185], v[18:19], off offset:1376
	ds_read_b128 v[80:83], v48 offset:38112
	s_waitcnt vmcnt(15) lgkmcnt(7)
	v_mfma_f32_32x32x16_bf16 v[2:17], v[84:87], v[186:189], v[2:17]
	global_load_dwordx4 v[186:189], v[18:19], off offset:1408
	ds_read_b128 v[84:87], v48 offset:42768
	s_waitcnt vmcnt(15) lgkmcnt(7)
	v_mfma_f32_32x32x16_bf16 v[2:17], v[88:91], v[190:193], v[2:17]
	global_load_dwordx4 v[190:193], v[18:19], off offset:1440
	ds_read_b128 v[88:91], v48 offset:42800
	s_waitcnt vmcnt(15) lgkmcnt(7)
	v_mfma_f32_32x32x16_bf16 v[2:17], v[92:95], v[200:203], v[2:17]
	global_load_dwordx4 v[200:203], v[18:19], off offset:1472
	ds_read_b128 v[92:95], v48 offset:42832
	s_waitcnt vmcnt(15) lgkmcnt(7)
	v_mfma_f32_32x32x16_bf16 v[2:17], v[96:99], v[204:207], v[2:17]
	global_load_dwordx4 v[204:207], v[18:19], off offset:1504
	ds_read_b128 v[96:99], v48 offset:42864
	s_waitcnt vmcnt(15) lgkmcnt(7)
	v_mfma_f32_32x32x16_bf16 v[2:17], v[208:211], v[138:141], v[2:17]
	global_load_dwordx4 v[138:141], v[18:19], off offset:1536
	ds_read_b128 v[208:211], v48 offset:47520
	s_waitcnt vmcnt(15) lgkmcnt(7)
	v_mfma_f32_32x32x16_bf16 v[2:17], v[212:215], v[142:145], v[2:17]
	global_load_dwordx4 v[142:145], v[18:19], off offset:1568
	ds_read_b128 v[212:215], v48 offset:47552
	s_waitcnt vmcnt(15) lgkmcnt(7)
	v_mfma_f32_32x32x16_bf16 v[2:17], v[216:219], v[146:149], v[2:17]
	global_load_dwordx4 v[146:149], v[18:19], off offset:1600
	ds_read_b128 v[216:219], v48 offset:47584
	s_waitcnt vmcnt(15) lgkmcnt(7)
	v_mfma_f32_32x32x16_bf16 v[2:17], v[80:83], v[150:153], v[2:17]
	global_load_dwordx4 v[150:153], v[18:19], off offset:1632
	ds_read_b128 v[80:83], v48 offset:47616
	s_waitcnt vmcnt(15) lgkmcnt(7)
	v_mfma_f32_32x32x16_bf16 v[2:17], v[84:87], v[154:157], v[2:17]
	global_load_dwordx4 v[154:157], v[18:19], off offset:1664
	ds_read_b128 v[84:87], v48 offset:52272
	s_waitcnt vmcnt(15) lgkmcnt(7)
	v_mfma_f32_32x32x16_bf16 v[2:17], v[88:91], v[158:161], v[2:17]
	global_load_dwordx4 v[158:161], v[18:19], off offset:1696
	ds_read_b128 v[88:91], v48 offset:52304
	s_waitcnt vmcnt(15) lgkmcnt(7)
	v_mfma_f32_32x32x16_bf16 v[2:17], v[92:95], v[162:165], v[2:17]
	global_load_dwordx4 v[162:165], v[18:19], off offset:1728
	ds_read_b128 v[92:95], v48 offset:52336
	s_waitcnt vmcnt(15) lgkmcnt(7)
	v_mfma_f32_32x32x16_bf16 v[2:17], v[96:99], v[166:169], v[2:17]
	global_load_dwordx4 v[166:169], v[18:19], off offset:1760
	ds_read_b128 v[96:99], v48 offset:52368
	s_waitcnt vmcnt(15) lgkmcnt(7)
	v_mfma_f32_32x32x16_bf16 v[2:17], v[208:211], v[170:173], v[2:17]
	global_load_dwordx4 v[170:173], v[18:19], off offset:1792
	ds_read_b128 v[208:211], v48 offset:57024
	s_waitcnt vmcnt(15) lgkmcnt(7)
; #define CMP_LOADW(dst, lb) { _Pragma("unroll") for (int q = 0; q < 4; ++q) _Pragma("unroll") for (int ks = 0; ks < 4; ++ks) dst[q][ks] = *(const GAS bf16x8*)(wrow + ((lb) + q) * 64 + 16 * ks); }
; #define CMP_MMA(src, lb) { _Pragma("unroll") for (int q = 0; q < 4; ++q) { const int ll = (lb) + q; const LAS unsigned char* xr = XS + ((ll & 15) * 33 + (ll >> 4) + r32) * XP + 16 * h; \
;             _Pragma("unroll") for (int ks = 0; ks < 4; ++ks) { const bf16x8 af = *(const LAS bf16x8*)(xr + 32 * ks); acc = __builtin_amdgcn_mfma_f32_32x32x16_bf16(af, src[q][ks], acc, 0, 0, 0); } } }
; __device__ __forceinline__ void compress_mfma_phase(Frame& F, int l, bf16* CMP) {
;     ...
;         { bf16x8 wa[4][4], wb[4][4]; const int l0 = 16 * lh;
;     ...
;           CMP_LOADW(wa, l0) CMP_LOADW(wb, l0 + 4) CMP_MMA(wa, l0) CMP_LOADW(wa, l0 + 8) CMP_MMA(wb, l0 + 4) CMP_LOADW(wb, l0 + 12) CMP_MMA(wa, l0 + 8) CMP_MMA(wb, l0 + 12)
;     ...
;         }
;         if (lh == 1) {
; #pragma unroll
;             for (int r = 0; r < 16; ++r) RED[((r & 3) + 8 * (r >> 2) + 4 * h) * 129 + 32 * ct + r32] = acc[r]; }
	v_mfma_f32_32x32x16_bf16 v[2:17], v[212:215], v[174:177], v[2:17]
	global_load_dwordx4 v[174:177], v[18:19], off offset:1824
	ds_read_b128 v[212:215], v48 offset:57056
	s_waitcnt vmcnt(15) lgkmcnt(7)
	v_mfma_f32_32x32x16_bf16 v[2:17], v[216:219], v[178:181], v[2:17]
	global_load_dwordx4 v[178:181], v[18:19], off offset:1856
	ds_read_b128 v[216:219], v48 offset:57088
	s_waitcnt vmcnt(15) lgkmcnt(7)
	v_mfma_f32_32x32x16_bf16 v[2:17], v[80:83], v[182:185], v[2:17]
	global_load_dwordx4 v[182:185], v[18:19], off offset:1888
	ds_read_b128 v[80:83], v48 offset:57120
	s_waitcnt vmcnt(15) lgkmcnt(7)
	v_mfma_f32_32x32x16_bf16 v[2:17], v[84:87], v[186:189], v[2:17]
	global_load_dwordx4 v[186:189], v[18:19], off offset:1920
	ds_read_b128 v[84:87], v48 offset:61776
	s_waitcnt vmcnt(15) lgkmcnt(7)
	v_mfma_f32_32x32x16_bf16 v[2:17], v[88:91], v[190:193], v[2:17]
	global_load_dwordx4 v[190:193], v[18:19], off offset:1952
	ds_read_b128 v[88:91], v48 offset:61808
	s_waitcnt vmcnt(15) lgkmcnt(7)
	v_mfma_f32_32x32x16_bf16 v[2:17], v[92:95], v[200:203], v[2:17]
	global_load_dwordx4 v[200:203], v[18:19], off offset:1984
	ds_read_b128 v[92:95], v48 offset:61840
	s_waitcnt vmcnt(15) lgkmcnt(7)
	v_mfma_f32_32x32x16_bf16 v[2:17], v[96:99], v[204:207], v[2:17]
	global_load_dwordx4 v[204:207], v[18:19], off offset:2016
	ds_read_b128 v[96:99], v48 offset:61872
	s_waitcnt vmcnt(15) lgkmcnt(7)
	v_mfma_f32_32x32x16_bf16 v[2:17], v[208:211], v[138:141], v[2:17]
	ds_read_b128 v[208:211], v49
	s_waitcnt vmcnt(14) lgkmcnt(7)
	v_mfma_f32_32x32x16_bf16 v[2:17], v[212:215], v[142:145], v[2:17]
	ds_read_b128 v[212:215], v50
	s_waitcnt vmcnt(13) lgkmcnt(7)
	v_mfma_f32_32x32x16_bf16 v[2:17], v[216:219], v[146:149], v[2:17]
	ds_read_b128 v[216:219], v51
	s_waitcnt vmcnt(12) lgkmcnt(7)
	v_mfma_f32_32x32x16_bf16 v[2:17], v[80:83], v[150:153], v[2:17]
	ds_read_b128 v[80:83], v52
	s_waitcnt vmcnt(11) lgkmcnt(7)
	v_mfma_f32_32x32x16_bf16 v[2:17], v[84:87], v[154:157], v[2:17]
	ds_read_b128 v[84:87], v53
	s_waitcnt vmcnt(10) lgkmcnt(7)
	v_mfma_f32_32x32x16_bf16 v[2:17], v[88:91], v[158:161], v[2:17]
	ds_read_b128 v[88:91], v54
	s_waitcnt vmcnt(9) lgkmcnt(7)
	v_mfma_f32_32x32x16_bf16 v[2:17], v[92:95], v[162:165], v[2:17]
	ds_read_b128 v[92:95], v55
	s_waitcnt vmcnt(8) lgkmcnt(7)
	v_mfma_f32_32x32x16_bf16 v[2:17], v[96:99], v[166:169], v[2:17]
	ds_read_b128 v[96:99], v56
	s_waitcnt vmcnt(7) lgkmcnt(7)
	v_mfma_f32_32x32x16_bf16 v[2:17], v[208:211], v[170:173], v[2:17]
	s_waitcnt vmcnt(6) lgkmcnt(6)
	v_mfma_f32_32x32x16_bf16 v[2:17], v[212:215], v[174:177], v[2:17]
	s_waitcnt vmcnt(5) lgkmcnt(5)
	v_mfma_f32_32x32x16_bf16 v[2:17], v[216:219], v[178:181], v[2:17]
	s_waitcnt vmcnt(4) lgkmcnt(4)
	v_mfma_f32_32x32x16_bf16 v[2:17], v[80:83], v[182:185], v[2:17]
	s_waitcnt vmcnt(3) lgkmcnt(3)
	v_mfma_f32_32x32x16_bf16 v[2:17], v[84:87], v[186:189], v[2:17]
	s_waitcnt vmcnt(2) lgkmcnt(2)
	v_mfma_f32_32x32x16_bf16 v[2:17], v[88:91], v[190:193], v[2:17]
	s_waitcnt vmcnt(1) lgkmcnt(1)
	v_mfma_f32_32x32x16_bf16 v[2:17], v[92:95], v[200:203], v[2:17]
	s_waitcnt vmcnt(0) lgkmcnt(0)
	v_mfma_f32_32x32x16_bf16 v[2:17], v[96:99], v[204:207], v[2:17]
	v_readlane_b32 s2, v246, 15
	v_readlane_b32 s3, v246, 16
	s_andn2_b64 vcc, exec, s[2:3]
	s_cbranch_vccnz .LBB0_381
	v_add_u32_e32 v0, 0x400, v78
	s_nop 9
	ds_write2_b32 v0, v4, v5 offset0:2 offset1:131
	v_add_u32_e32 v0, 0x1000, v78
	ds_write2_b32 v0, v6, v7 offset0:8 offset1:137
	v_add_u32_e32 v0, 0x1400, v78
	ds_write2_b32 v0, v8, v9 offset0:10 offset1:139
	v_add_u32_e32 v0, 0x2000, v78
	ds_write2_b32 v0, v10, v11 offset0:16 offset1:145
	v_add_u32_e32 v0, 0x2400, v78
	ds_write2_b32 v0, v12, v13 offset0:18 offset1:147
	v_add_u32_e32 v0, 0x3000, v78
	ds_write2_b32 v0, v14, v15 offset0:24 offset1:153
	v_add_u32_e32 v0, 0x3400, v78
	ds_write2_b32 v78, v2, v3 offset1:129
	ds_write2_b32 v0, v16, v17 offset0:26 offset1:155
